# speedup vs baseline: 1.0275x; 1.0275x over previous
.LBB0_4:
	v_lshrrev_b32_e32 v4, 13, v2
	v_lshrrev_b32_e32 v6, 3, v0
	v_ashrrev_i32_e32 v3, 17, v2
	v_and_b32_e32 v4, 14, v4
	v_and_b32_e32 v6, 14, v6
	v_add_u32_e32 v4, v4, v3
	v_add_u32_e32 v6, v3, v6
	s_load_dwordx2 s[2:3], s[0:1], 0x0
	v_ashrrev_i32_e32 v5, 31, v4
	v_ashrrev_i32_e32 v7, 31, v6
	v_lshlrev_b64 v[4:5], 11, v[4:5]
	v_lshlrev_b64 v[6:7], 7, v[6:7]
	v_lshrrev_b32_e32 v1, 7, v2
	v_lshl_add_u64 v[4:5], v[4:5], 0, v[6:7]
	s_movk_i32 s4, 0x7f
	v_and_or_b32 v4, v1, s4, v4
	v_lshlrev_b64 v[4:5], 9, v[4:5]
	v_lshlrev_b32_e32 v0, 5, v0
	s_waitcnt lgkmcnt(0)
	v_lshl_add_u64 v[4:5], s[2:3], 0, v[4:5]
	v_and_b32_e32 v0, 0x1e0, v0
	v_mov_b32_e32 v1, 0
	v_lshl_add_u64 v[0:1], v[4:5], 0, v[0:1]
	global_load_dwordx4 v[4:7], v[0:1], off
	global_load_dwordx4 v[8:11], v[0:1], off offset:16
	s_load_dwordx2 s[0:1], s[0:1], 0x10
	v_ashrrev_i32_e32 v3, 31, v2
	s_waitcnt lgkmcnt(0)
	v_lshl_add_u64 v[0:1], v[2:3], 4, s[0:1]
	s_waitcnt vmcnt(1)
	v_cvt_pk_bf16_f32 v4, v4, v5
	v_cvt_pk_bf16_f32 v5, v6, v7
	s_waitcnt vmcnt(0)
	v_cvt_pk_bf16_f32 v6, v8, v9
	v_cvt_pk_bf16_f32 v7, v10, v11
	global_store_dwordx4 v[0:1], v[4:7], off
	s_endpgm

_Z11gemm_kernelPKfPKDF16bS0_Pf:
	s_and_b32 s3, s2, 7
	s_ashr_i32 s14, s2, 3
	s_lshl_b32 s12, s3, 6
	s_load_dwordx8 s[4:11], s[0:1], 0x0
	s_add_i32 s12, s12, s14
	s_bfe_u32 s18, s2, 0x10002
	s_lshl_b32 s2, s12, 6
	s_lshl_b32 s13, s18, 14
	s_and_b32 s2, s2, 0x3f00
	v_lshrrev_b32_e32 v52, 6, v0
	v_and_b32_e32 v50, 15, v0
	v_bfe_u32 v51, v0, 4, 2
	v_bfe_u32 v1, v0, 3, 3
	s_or_b32 s2, s2, s13
	v_lshl_or_b32 v102, v52, 2, v51
	v_lshl_or_b32 v104, v52, 3, v1
	v_lshlrev_b32_e32 v1, 4, v50
	s_lshl_b32 s15, s2, 9
	s_waitcnt lgkmcnt(0)
	s_mov_b64 s[0:1], s[6:7]
	s_and_b32 s5, s5, 0xffff
	s_mov_b32 s7, 0x20000
	s_brev_b32 s6, -2
	v_lshl_or_b32 v1, v102, 9, v1
	s_or_b32 s2, s15, 0x4000
	s_lshl_b32 s14, s14, 8
	v_lshlrev_b32_e32 v103, 3, v0
	buffer_load_dwordx4 v[54:57], v1, s[4:7], s15 offen sc0 nt
	buffer_load_dwordx4 v[58:61], v1, s[4:7], s2 offen sc0 nt
	s_or_b32 s2, s15, 0x8000
	s_or_b32 s3, s15, 0xc000
	s_lshl_b32 s19, s18, 10
	s_and_b32 s20, s14, 0x300
	v_and_b32_e32 v105, 56, v103
	buffer_load_dwordx4 v[62:65], v1, s[4:7], s2 offen sc0 nt
	buffer_load_dwordx4 v[66:69], v1, s[4:7], s3 offen sc0 nt
	s_or_b32 s2, s15, 0x10000
	s_or_b32 s3, s15, 0x14000
	s_or_b32 s14, s19, s20
	v_lshlrev_b32_e32 v106, 1, v105
	buffer_load_dwordx4 v[70:73], v1, s[4:7], s2 offen sc0 nt
	buffer_load_dwordx4 v[74:77], v1, s[4:7], s3 offen sc0 nt
	s_or_b32 s2, s15, 0x18000
	s_or_b32 s3, s15, 0x1c000
	s_lshl_b32 s14, s14, 11
	buffer_load_dwordx4 v[78:81], v1, s[4:7], s2 offen sc0 nt
	buffer_load_dwordx4 v[82:85], v1, s[4:7], s3 offen sc0 nt
	s_and_b32 s1, s1, 0xffff
	s_mov_b32 s2, s6
	s_mov_b32 s3, s7
	v_lshl_or_b32 v188, v104, 11, v106
	s_or_b32 s16, s14, 0x20000
	buffer_load_dwordx4 v[86:89], v188, s[0:3], s14 offen sc1
	buffer_load_dwordx4 v[90:93], v188, s[0:3], s16 offen sc1
	s_or_b32 s16, s14, 0x40000
	s_or_b32 s17, s14, 0x60000
	buffer_load_dwordx4 v[94:97], v188, s[0:3], s16 offen sc1
	buffer_load_dwordx4 v[98:101], v188, s[0:3], s17 offen sc1
	s_or_b32 s16, s15, 0x100
	s_or_b32 s17, s15, 0x4100
	buffer_load_dwordx4 v[10:13], v1, s[4:7], s16 offen sc0 nt
	buffer_load_dwordx4 v[18:21], v1, s[4:7], s17 offen sc0 nt
	s_or_b32 s16, s15, 0x8100
	s_or_b32 s17, s15, 0xc100
	buffer_load_dwordx4 v[22:25], v1, s[4:7], s16 offen sc0 nt
	buffer_load_dwordx4 v[30:33], v1, s[4:7], s17 offen sc0 nt
	s_or_b32 s16, s15, 0x10100
	s_or_b32 s17, s15, 0x14100
	buffer_load_dwordx4 v[34:37], v1, s[4:7], s16 offen sc0 nt
	buffer_load_dwordx4 v[38:41], v1, s[4:7], s17 offen sc0 nt
	s_or_b32 s16, s15, 0x18100
	s_or_b32 s15, s15, 0x1c100
	buffer_load_dwordx4 v[42:45], v1, s[4:7], s16 offen sc0 nt
	buffer_load_dwordx4 v[46:49], v1, s[4:7], s15 offen sc0 nt
	s_or_b32 s15, s14, 0x80
	s_or_b32 s16, s14, 0x20080
	buffer_load_dwordx4 v[2:5], v188, s[0:3], s15 offen sc1
	buffer_load_dwordx4 v[6:9], v188, s[0:3], s16 offen sc1
	s_or_b32 s15, s14, 0x40080
	s_or_b32 s16, s14, 0x60080
	buffer_load_dwordx4 v[14:17], v188, s[0:3], s15 offen sc1
	buffer_load_dwordx4 v[26:29], v188, s[0:3], s16 offen sc1
	v_lshrrev_b32_e32 v107, 7, v0
	v_bfe_u32 v108, v0, 3, 1
	v_lshlrev_b32_e32 v102, 6, v102
	s_movk_i32 s2, 0x3c0
	v_and_or_b32 v102, v102, s2, v105
	v_lshrrev_b32_e32 v105, 2, v0
	v_and_or_b32 v107, v107, 2, v108
	v_and_b32_e32 v105, 32, v105
	v_lshlrev_b32_e32 v107, 10, v107
	v_bfe_u32 v103, v103, 5, 1
	v_lshlrev_b32_e32 v104, 6, v104
	v_and_b32_e32 v106, 48, v106
	v_bitop3_b32 v189, v102, v107, v105 bitop3:0xde
	v_and_or_b32 v103, v52, 6, v103
	v_and_or_b32 v104, v104, s2, v106
	v_lshrrev_b32_e32 v106, 1, v0
	v_lshlrev_b32_e32 v103, 10, v103
	v_and_b32_e32 v106, 32, v106
	v_bitop3_b32 v190, v104, v103, v106 bitop3:0xde
	v_lshrrev_b32_e32 v53, 8, v0
	s_movk_i32 s15, 0x4000
	s_mov_b32 s16, 0x8000
	s_mov_b32 s17, 0xc000
	s_waitcnt vmcnt(23)
	v_cvt_pk_bf16_f32 v57, v56, v57
	v_cvt_pk_bf16_f32 v56, v54, v55
	s_waitcnt vmcnt(22)
	v_cvt_pk_bf16_f32 v55, v60, v61
	v_cvt_pk_bf16_f32 v54, v58, v59
	ds_write2st64_b64 v189, v[56:57], v[54:55] offset1:8
	s_waitcnt vmcnt(21)
	v_cvt_pk_bf16_f32 v55, v64, v65
	v_cvt_pk_bf16_f32 v54, v62, v63
	s_waitcnt vmcnt(20)
	v_cvt_pk_bf16_f32 v57, v68, v69
	v_cvt_pk_bf16_f32 v56, v66, v67
	ds_write2st64_b64 v189, v[54:55], v[56:57] offset0:16 offset1:24
	s_waitcnt vmcnt(19)
	v_cvt_pk_bf16_f32 v55, v72, v73
	v_cvt_pk_bf16_f32 v54, v70, v71
	s_waitcnt vmcnt(18)
	v_cvt_pk_bf16_f32 v57, v76, v77
	v_cvt_pk_bf16_f32 v56, v74, v75
	ds_write2st64_b64 v189, v[54:55], v[56:57] offset0:32 offset1:40
	s_waitcnt vmcnt(17)
	v_cvt_pk_bf16_f32 v55, v80, v81
	v_cvt_pk_bf16_f32 v54, v78, v79
	s_waitcnt vmcnt(16)
	v_cvt_pk_bf16_f32 v57, v84, v85
	v_cvt_pk_bf16_f32 v56, v82, v83
	ds_write2st64_b64 v189, v[54:55], v[56:57] offset0:48 offset1:56
	s_waitcnt vmcnt(15)
	ds_write_b128 v190, v[86:89] offset:32768
	s_waitcnt vmcnt(14)
	ds_write_b128 v190, v[90:93] offset:40960
	s_waitcnt vmcnt(13)
	ds_write_b128 v190, v[94:97] offset:49152
	s_waitcnt vmcnt(12)
	ds_write_b128 v190, v[98:101] offset:57344
	s_waitcnt lgkmcnt(0)
	s_barrier
	v_cmp_eq_u32_e32 vcc, 1, v53
	s_and_saveexec_b64 s[2:3], vcc
	s_cbranch_execz .LBB1_2
	s_barrier
.LBB1_2:
	s_or_b64 exec, exec, s[2:3]
	v_and_b32_e32 v52, 3, v52
	v_and_b32_e32 v54, 48, v0
	v_lshlrev_b32_e32 v55, 2, v0
	v_lshl_or_b32 v54, v50, 6, v54
	v_and_b32_e32 v55, 32, v55
	v_lshlrev_b32_e32 v56, 14, v53
	v_lshlrev_b32_e32 v57, 13, v52
	v_lshl_or_b32 v52, v52, 6, s20
	v_lshlrev_b32_e32 v51, 2, v51
	s_movk_i32 s2, 0x4c
	v_bitop3_b32 v191, v54, v57, v55 bitop3:0xde
	v_bitop3_b32 v192, v54, v56, v55 bitop3:0xde
	v_or_b32_e32 v54, v52, v51
	v_bitop3_b32 v51, v52, s2, v51 bitop3:0xc8
	v_lshrrev_b32_e32 v52, 6, v52
	s_lshl_b32 s2, s19, 2
	v_and_or_b32 v52, v52, 14, s18
	v_lshlrev_b32_e32 v182, 2, v51
	v_mov_b32_e32 v183, 0
	s_add_u32 s2, s8, s2
	v_lshlrev_b32_e32 v52, 14, v52
	v_lshlrev_b32_e32 v53, 7, v53
	v_lshl_add_u64 v[184:185], s[10:11], 0, v[182:183]
	s_addc_u32 s3, s9, 0
	v_lshlrev_b32_e32 v182, 2, v54
	v_or3_b32 v193, v53, v52, v50
	s_mov_b32 s18, 0
	v_lshl_add_u64 v[186:187], s[2:3], 0, v[182:183]
	s_mov_b32 s2, s6
	s_mov_b32 s3, s7
	s_movk_i32 s8, 0x2000
	s_movk_i32 s9, 0x6000
	s_mov_b32 s10, 0xa000
	s_mov_b32 s11, 0xe000
	s_mov_b32 s19, 0
	s_mov_b32 s20, 0
	v_mov_b32_e32 v50, v183
	v_mov_b32_e32 v51, v183
	v_mov_b32_e32 v52, v183
	v_mov_b32_e32 v53, v183
	v_mov_b32_e32 v58, v183
	v_mov_b32_e32 v59, v183
	v_mov_b32_e32 v60, v183
	v_mov_b32_e32 v61, v183
	v_mov_b32_e32 v66, v183
	v_mov_b32_e32 v67, v183
	v_mov_b32_e32 v68, v183
	v_mov_b32_e32 v69, v183
	v_mov_b32_e32 v78, v183
	v_mov_b32_e32 v79, v183
	v_mov_b32_e32 v80, v183
	v_mov_b32_e32 v81, v183
	v_mov_b32_e32 v54, v183
	v_mov_b32_e32 v55, v183
	v_mov_b32_e32 v56, v183
	v_mov_b32_e32 v57, v183
	v_mov_b32_e32 v70, v183
	v_mov_b32_e32 v71, v183
	v_mov_b32_e32 v72, v183
	v_mov_b32_e32 v73, v183
	v_mov_b32_e32 v86, v183
	v_mov_b32_e32 v87, v183
	v_mov_b32_e32 v88, v183
	v_mov_b32_e32 v89, v183
	v_mov_b32_e32 v94, v183
	v_mov_b32_e32 v95, v183
	v_mov_b32_e32 v96, v183
	v_mov_b32_e32 v97, v183
	v_mov_b32_e32 v62, v183
	v_mov_b32_e32 v63, v183
	v_mov_b32_e32 v64, v183
	v_mov_b32_e32 v65, v183
	v_mov_b32_e32 v82, v183
	v_mov_b32_e32 v83, v183
	v_mov_b32_e32 v84, v183
	v_mov_b32_e32 v85, v183
	v_mov_b32_e32 v102, v183
	v_mov_b32_e32 v103, v183
	v_mov_b32_e32 v104, v183
	v_mov_b32_e32 v105, v183
	v_mov_b32_e32 v110, v183
	v_mov_b32_e32 v111, v183
	v_mov_b32_e32 v112, v183
	v_mov_b32_e32 v113, v183
	v_mov_b32_e32 v74, v183
	v_mov_b32_e32 v75, v183
	v_mov_b32_e32 v76, v183
	v_mov_b32_e32 v77, v183
	v_mov_b32_e32 v98, v183
	v_mov_b32_e32 v99, v183
	v_mov_b32_e32 v100, v183
	v_mov_b32_e32 v101, v183
	v_mov_b32_e32 v118, v183
	v_mov_b32_e32 v119, v183
	v_mov_b32_e32 v120, v183
	v_mov_b32_e32 v121, v183
	v_mov_b32_e32 v126, v183
	v_mov_b32_e32 v127, v183
	v_mov_b32_e32 v128, v183
	v_mov_b32_e32 v129, v183
	v_mov_b32_e32 v90, v183
	v_mov_b32_e32 v91, v183
	v_mov_b32_e32 v92, v183
	v_mov_b32_e32 v93, v183
	v_mov_b32_e32 v114, v183
	v_mov_b32_e32 v115, v183
	v_mov_b32_e32 v116, v183
	v_mov_b32_e32 v117, v183
	v_mov_b32_e32 v134, v183
	v_mov_b32_e32 v135, v183
	v_mov_b32_e32 v136, v183
	v_mov_b32_e32 v137, v183
	v_mov_b32_e32 v138, v183
	v_mov_b32_e32 v139, v183
	v_mov_b32_e32 v140, v183
	v_mov_b32_e32 v141, v183
	v_mov_b32_e32 v106, v183
	v_mov_b32_e32 v107, v183
	v_mov_b32_e32 v108, v183
	v_mov_b32_e32 v109, v183
	v_mov_b32_e32 v130, v183
	v_mov_b32_e32 v131, v183
	v_mov_b32_e32 v132, v183
	v_mov_b32_e32 v133, v183
	v_mov_b32_e32 v150, v183
	v_mov_b32_e32 v151, v183
	v_mov_b32_e32 v152, v183
	v_mov_b32_e32 v153, v183
	v_mov_b32_e32 v154, v183
	v_mov_b32_e32 v155, v183
	v_mov_b32_e32 v156, v183
	v_mov_b32_e32 v157, v183
	v_mov_b32_e32 v122, v183
	v_mov_b32_e32 v123, v183
	v_mov_b32_e32 v124, v183
	v_mov_b32_e32 v125, v183
	v_mov_b32_e32 v146, v183
	v_mov_b32_e32 v147, v183
	v_mov_b32_e32 v148, v183
	v_mov_b32_e32 v149, v183
	v_mov_b32_e32 v162, v183
	v_mov_b32_e32 v163, v183
	v_mov_b32_e32 v164, v183
	v_mov_b32_e32 v165, v183
	v_mov_b32_e32 v166, v183
	v_mov_b32_e32 v167, v183
	v_mov_b32_e32 v168, v183
	v_mov_b32_e32 v169, v183
	v_mov_b32_e32 v142, v183
	v_mov_b32_e32 v143, v183
	v_mov_b32_e32 v144, v183
	v_mov_b32_e32 v145, v183
	v_mov_b32_e32 v158, v183
	v_mov_b32_e32 v159, v183
	v_mov_b32_e32 v160, v183
	v_mov_b32_e32 v161, v183
	v_mov_b32_e32 v170, v183
	v_mov_b32_e32 v171, v183
	v_mov_b32_e32 v172, v183
	v_mov_b32_e32 v173, v183
	v_mov_b32_e32 v174, v183
	v_mov_b32_e32 v175, v183
	v_mov_b32_e32 v176, v183
	v_mov_b32_e32 v177, v183
	s_branch .LBB1_4
.LBB1_3:
	s_waitcnt lgkmcnt(0)
	s_barrier
	s_add_i32 s20, s20, 1
	s_add_i32 s18, s18, 2
	s_cmp_eq_u32 s20, 32
	s_cbranch_scc1 .LBB1_6
.LBB1_4:
	v_add_u32_e32 v182, s19, v191
	v_add_u32_e32 v238, s19, v192
	ds_read_b128 v[178:181], v182 offset:32768
	ds_read_b128 v[194:197], v182 offset:34816
	ds_read_b128 v[198:201], v182 offset:36864
	ds_read_b128 v[202:205], v182 offset:38912
	ds_read_b128 v[206:209], v238
	ds_read_b128 v[210:213], v238 offset:2048
	ds_read_b128 v[214:217], v238 offset:4096
	ds_read_b128 v[218:221], v238 offset:6144
	ds_read_b128 v[222:225], v238 offset:8192
	ds_read_b128 v[226:229], v238 offset:10240
	ds_read_b128 v[230:233], v238 offset:12288
	ds_read_b128 v[234:237], v238 offset:14336
	s_min_u32 s21, s20, 29
	s_xor_b32 s19, s19, 0x10000
	v_add_u32_e32 v239, s19, v189
	s_waitcnt vmcnt(11)
	v_cvt_pk_bf16_f32 v13, v12, v13
	v_cvt_pk_bf16_f32 v12, v10, v11
	s_waitcnt vmcnt(10)
	v_cvt_pk_bf16_f32 v11, v20, v21
	v_cvt_pk_bf16_f32 v10, v18, v19
	ds_write2st64_b64 v239, v[12:13], v[10:11] offset1:8
	s_waitcnt vmcnt(9)
	v_cvt_pk_bf16_f32 v11, v24, v25
	v_cvt_pk_bf16_f32 v10, v22, v23
	s_waitcnt vmcnt(8)
	v_cvt_pk_bf16_f32 v13, v32, v33
	v_cvt_pk_bf16_f32 v12, v30, v31
	ds_write2st64_b64 v239, v[10:11], v[12:13] offset0:16 offset1:24
	s_waitcnt vmcnt(7)
	v_cvt_pk_bf16_f32 v11, v36, v37
	v_cvt_pk_bf16_f32 v10, v34, v35
	s_waitcnt vmcnt(6)
	v_cvt_pk_bf16_f32 v13, v40, v41
	v_cvt_pk_bf16_f32 v12, v38, v39
	ds_write2st64_b64 v239, v[10:11], v[12:13] offset0:32 offset1:40
	s_waitcnt vmcnt(5)
	v_cvt_pk_bf16_f32 v11, v44, v45
	v_cvt_pk_bf16_f32 v10, v42, v43
	s_waitcnt vmcnt(4)
	v_cvt_pk_bf16_f32 v13, v48, v49
	v_cvt_pk_bf16_f32 v12, v46, v47
	ds_write2st64_b64 v239, v[10:11], v[12:13] offset0:48 offset1:56
	s_waitcnt lgkmcnt(0)
	s_add_i32 s21, s21, 2
	s_barrier
	s_setprio 1
	s_lshl_b32 s22, s21, 1
	s_and_b32 s22, s22, 0x60
	s_add_i32 s22, s22, s12
	s_lshl_b32 s22, s22, 6
	s_and_b32 s22, s22, 0x3f00
	s_or_b32 s22, s22, s13
	s_lshl_b32 s23, s21, 23
	s_lshl_b32 s22, s22, 9
	s_and_b32 s23, s23, 0x7000000
	s_or_b32 s22, s22, s23
	s_lshl_b32 s23, s21, 8
	s_and_b32 s23, s23, 0x100
	s_or_b32 s22, s22, s23
	s_or_b32 s23, s22, 0x4000
	s_waitcnt lgkmcnt(11)
	v_mfma_f32_16x16x32_bf16 v[174:177], v[178:181], v[206:209], v[174:177]
	v_mfma_f32_16x16x32_bf16 v[170:173], v[194:197], v[206:209], v[170:173]
	v_mfma_f32_16x16x32_bf16 v[158:161], v[198:201], v[206:209], v[158:161]
	buffer_load_dwordx4 v[10:13], v1, s[4:7], s22 offen sc0 nt
	v_mfma_f32_16x16x32_bf16 v[142:145], v[202:205], v[206:209], v[142:145]
	s_waitcnt lgkmcnt(10)
	v_mfma_f32_16x16x32_bf16 v[166:169], v[178:181], v[210:213], v[166:169]
	v_mfma_f32_16x16x32_bf16 v[162:165], v[194:197], v[210:213], v[162:165]
	v_mfma_f32_16x16x32_bf16 v[146:149], v[198:201], v[210:213], v[146:149]
	buffer_load_dwordx4 v[18:21], v1, s[4:7], s23 offen sc0 nt
	s_or_b32 s23, s22, 0x8000
	v_mfma_f32_16x16x32_bf16 v[122:125], v[202:205], v[210:213], v[122:125]
	s_waitcnt lgkmcnt(9)
	v_mfma_f32_16x16x32_bf16 v[154:157], v[178:181], v[214:217], v[154:157]
	v_mfma_f32_16x16x32_bf16 v[150:153], v[194:197], v[214:217], v[150:153]
	v_mfma_f32_16x16x32_bf16 v[130:133], v[198:201], v[214:217], v[130:133]
	buffer_load_dwordx4 v[22:25], v1, s[4:7], s23 offen sc0 nt
	s_or_b32 s23, s22, 0xc000
	v_mfma_f32_16x16x32_bf16 v[106:109], v[202:205], v[214:217], v[106:109]
	s_waitcnt lgkmcnt(8)
	v_mfma_f32_16x16x32_bf16 v[138:141], v[178:181], v[218:221], v[138:141]
	v_mfma_f32_16x16x32_bf16 v[134:137], v[194:197], v[218:221], v[134:137]
	v_mfma_f32_16x16x32_bf16 v[114:117], v[198:201], v[218:221], v[114:117]
	buffer_load_dwordx4 v[30:33], v1, s[4:7], s23 offen sc0 nt
	s_or_b32 s23, s22, 0x10000
	v_mfma_f32_16x16x32_bf16 v[90:93], v[202:205], v[218:221], v[90:93]
	s_waitcnt lgkmcnt(7)
	v_mfma_f32_16x16x32_bf16 v[126:129], v[178:181], v[222:225], v[126:129]
	v_mfma_f32_16x16x32_bf16 v[118:121], v[194:197], v[222:225], v[118:121]
	v_mfma_f32_16x16x32_bf16 v[98:101], v[198:201], v[222:225], v[98:101]
	buffer_load_dwordx4 v[34:37], v1, s[4:7], s23 offen sc0 nt
	s_or_b32 s23, s22, 0x14000
	v_mfma_f32_16x16x32_bf16 v[74:77], v[202:205], v[222:225], v[74:77]
	s_waitcnt lgkmcnt(6)
	v_mfma_f32_16x16x32_bf16 v[110:113], v[178:181], v[226:229], v[110:113]
	v_mfma_f32_16x16x32_bf16 v[102:105], v[194:197], v[226:229], v[102:105]
	v_mfma_f32_16x16x32_bf16 v[82:85], v[198:201], v[226:229], v[82:85]
	buffer_load_dwordx4 v[38:41], v1, s[4:7], s23 offen sc0 nt
	s_or_b32 s23, s22, 0x18000
	s_or_b32 s22, s22, 0x1c000
	v_mfma_f32_16x16x32_bf16 v[62:65], v[202:205], v[226:229], v[62:65]
	s_waitcnt lgkmcnt(5)
	v_mfma_f32_16x16x32_bf16 v[94:97], v[178:181], v[230:233], v[94:97]
	v_mfma_f32_16x16x32_bf16 v[86:89], v[194:197], v[230:233], v[86:89]
	v_mfma_f32_16x16x32_bf16 v[70:73], v[198:201], v[230:233], v[70:73]
	buffer_load_dwordx4 v[42:45], v1, s[4:7], s23 offen sc0 nt
	v_mfma_f32_16x16x32_bf16 v[54:57], v[202:205], v[230:233], v[54:57]
	s_waitcnt lgkmcnt(4)
	v_mfma_f32_16x16x32_bf16 v[78:81], v[178:181], v[234:237], v[78:81]
	v_mfma_f32_16x16x32_bf16 v[66:69], v[194:197], v[234:237], v[66:69]
	v_mfma_f32_16x16x32_bf16 v[58:61], v[198:201], v[234:237], v[58:61]
	buffer_load_dwordx4 v[46:49], v1, s[4:7], s22 offen sc0 nt
	v_mfma_f32_16x16x32_bf16 v[50:53], v[202:205], v[234:237], v[50:53]
	s_setprio 0
	s_waitcnt lgkmcnt(0)
	s_barrier
	ds_read_b128 v[178:181], v182 offset:33792
	ds_read_b128 v[194:197], v182 offset:35840
	ds_read_b128 v[198:201], v182 offset:37888
	ds_read_b128 v[202:205], v182 offset:39936
	ds_read_b128 v[206:209], v238 offset:1024
	ds_read_b128 v[210:213], v238 offset:3072
	ds_read_b128 v[214:217], v238 offset:5120
	ds_read_b128 v[218:221], v238 offset:7168
	ds_read_b128 v[222:225], v238 offset:9216
	ds_read_b128 v[226:229], v238 offset:11264
	ds_read_b128 v[230:233], v238 offset:13312
	ds_read_b128 v[234:237], v238 offset:15360
	v_add_u32_e32 v182, s19, v190
	s_waitcnt vmcnt(11)
	ds_write_b128 v182, v[2:5] offset:32768
	s_waitcnt vmcnt(10)
	ds_write_b128 v182, v[6:9] offset:40960
	s_waitcnt vmcnt(9)
	ds_write_b128 v182, v[14:17] offset:49152
	s_waitcnt vmcnt(8)
	ds_write_b128 v182, v[26:29] offset:57344
	s_waitcnt lgkmcnt(0)
	s_barrier
	s_setprio 1
	s_lshl_b32 s21, s21, 7
	s_and_b32 s21, s21, 0x780
	s_or_b32 s21, s21, s14
	s_or_b32 s22, s21, 0x20000
	s_waitcnt lgkmcnt(11)
	v_mfma_f32_16x16x32_bf16 v[174:177], v[178:181], v[206:209], v[174:177]
	v_mfma_f32_16x16x32_bf16 v[170:173], v[194:197], v[206:209], v[170:173]
	v_mfma_f32_16x16x32_bf16 v[158:161], v[198:201], v[206:209], v[158:161]
	v_mfma_f32_16x16x32_bf16 v[142:145], v[202:205], v[206:209], v[142:145]
	s_waitcnt lgkmcnt(10)
	v_mfma_f32_16x16x32_bf16 v[166:169], v[178:181], v[210:213], v[166:169]
	v_mfma_f32_16x16x32_bf16 v[162:165], v[194:197], v[210:213], v[162:165]
	buffer_load_dwordx4 v[2:5], v188, s[0:3], s21 offen sc1
	v_mfma_f32_16x16x32_bf16 v[146:149], v[198:201], v[210:213], v[146:149]
	v_mfma_f32_16x16x32_bf16 v[122:125], v[202:205], v[210:213], v[122:125]
	s_waitcnt lgkmcnt(9)
	v_mfma_f32_16x16x32_bf16 v[154:157], v[178:181], v[214:217], v[154:157]
	v_mfma_f32_16x16x32_bf16 v[150:153], v[194:197], v[214:217], v[150:153]
	v_mfma_f32_16x16x32_bf16 v[130:133], v[198:201], v[214:217], v[130:133]
	v_mfma_f32_16x16x32_bf16 v[106:109], v[202:205], v[214:217], v[106:109]
	s_waitcnt lgkmcnt(8)
	v_mfma_f32_16x16x32_bf16 v[138:141], v[178:181], v[218:221], v[138:141]
	v_mfma_f32_16x16x32_bf16 v[134:137], v[194:197], v[218:221], v[134:137]
	buffer_load_dwordx4 v[6:9], v188, s[0:3], s22 offen sc1
	s_or_b32 s22, s21, 0x40000
	s_or_b32 s21, s21, 0x60000
	v_mfma_f32_16x16x32_bf16 v[114:117], v[198:201], v[218:221], v[114:117]
	v_mfma_f32_16x16x32_bf16 v[90:93], v[202:205], v[218:221], v[90:93]
	s_waitcnt lgkmcnt(7)
	v_mfma_f32_16x16x32_bf16 v[126:129], v[178:181], v[222:225], v[126:129]
	v_mfma_f32_16x16x32_bf16 v[118:121], v[194:197], v[222:225], v[118:121]
	v_mfma_f32_16x16x32_bf16 v[98:101], v[198:201], v[222:225], v[98:101]
	v_mfma_f32_16x16x32_bf16 v[74:77], v[202:205], v[222:225], v[74:77]
	s_waitcnt lgkmcnt(6)
	v_mfma_f32_16x16x32_bf16 v[110:113], v[178:181], v[226:229], v[110:113]
	v_mfma_f32_16x16x32_bf16 v[102:105], v[194:197], v[226:229], v[102:105]
	buffer_load_dwordx4 v[14:17], v188, s[0:3], s22 offen sc1
	v_mfma_f32_16x16x32_bf16 v[82:85], v[198:201], v[226:229], v[82:85]
	v_mfma_f32_16x16x32_bf16 v[62:65], v[202:205], v[226:229], v[62:65]
	s_waitcnt lgkmcnt(5)
	v_mfma_f32_16x16x32_bf16 v[94:97], v[178:181], v[230:233], v[94:97]
	v_mfma_f32_16x16x32_bf16 v[86:89], v[194:197], v[230:233], v[86:89]
	v_mfma_f32_16x16x32_bf16 v[70:73], v[198:201], v[230:233], v[70:73]
	v_mfma_f32_16x16x32_bf16 v[54:57], v[202:205], v[230:233], v[54:57]
	s_waitcnt lgkmcnt(4)
	v_mfma_f32_16x16x32_bf16 v[78:81], v[178:181], v[234:237], v[78:81]
	v_mfma_f32_16x16x32_bf16 v[66:69], v[194:197], v[234:237], v[66:69]
	buffer_load_dwordx4 v[26:29], v188, s[0:3], s21 offen sc1
	v_mfma_f32_16x16x32_bf16 v[58:61], v[198:201], v[234:237], v[58:61]
	v_mfma_f32_16x16x32_bf16 v[50:53], v[202:205], v[234:237], v[50:53]
	s_setprio 0
	s_and_b32 s21, s20, 15
	s_cmp_lg_u32 s21, 15
	s_cbranch_scc1 .LBB1_3
	global_load_dwordx4 v[178:181], v[186:187], off
	global_load_dwordx4 v[194:197], v[186:187], off offset:64
	global_load_dwordx4 v[198:201], v[186:187], off offset:128
	global_load_dwordx4 v[202:205], v[186:187], off offset:192
	s_and_b32 s21, s18, 32
	s_add_i32 s21, s21, s12
	s_lshl_b32 s21, s21, 6
	s_and_b32 s21, s21, 0x3f00
	v_add_lshl_u32 v182, v193, s21, 9
	v_lshl_add_u64 v[206:207], v[184:185], 0, v[182:183]
	v_add_co_u32_e32 v208, vcc, s8, v206
	s_waitcnt vmcnt(3)
	v_pk_add_f32 v[176:177], v[180:181], v[176:177]
	v_addc_co_u32_e32 v209, vcc, 0, v207, vcc
	v_add_co_u32_e32 v210, vcc, s15, v206
	v_pk_add_f32 v[174:175], v[178:179], v[174:175]
	s_nop 0
	v_addc_co_u32_e32 v211, vcc, 0, v207, vcc
	v_add_co_u32_e32 v212, vcc, s9, v206
	s_waitcnt vmcnt(2)
	v_pk_add_f32 v[68:69], v[196:197], v[68:69]
	v_addc_co_u32_e32 v213, vcc, 0, v207, vcc
	v_add_co_u32_e32 v214, vcc, s16, v206
	v_pk_add_f32 v[66:67], v[194:195], v[66:67]
	s_nop 0
	v_addc_co_u32_e32 v215, vcc, 0, v207, vcc
	v_add_co_u32_e32 v216, vcc, s10, v206
	v_pk_add_f32 v[168:169], v[180:181], v[168:169]
	s_nop 0
	v_addc_co_u32_e32 v217, vcc, 0, v207, vcc
	v_add_co_u32_e32 v218, vcc, s17, v206
	v_pk_add_f32 v[166:167], v[178:179], v[166:167]
	s_nop 0
	v_addc_co_u32_e32 v219, vcc, 0, v207, vcc
	v_add_co_u32_e32 v220, vcc, s11, v206
	v_pk_add_f32 v[156:157], v[180:181], v[156:157]
	s_nop 0
	v_addc_co_u32_e32 v221, vcc, 0, v207, vcc
	v_pk_add_f32 v[154:155], v[178:179], v[154:155]
	v_pk_add_f32 v[140:141], v[180:181], v[140:141]
	v_pk_add_f32 v[138:139], v[178:179], v[138:139]
	v_pk_add_f32 v[128:129], v[180:181], v[128:129]
	v_pk_add_f32 v[126:127], v[178:179], v[126:127]
	v_pk_add_f32 v[112:113], v[180:181], v[112:113]
	v_pk_add_f32 v[110:111], v[178:179], v[110:111]
	v_pk_add_f32 v[96:97], v[180:181], v[96:97]
	v_pk_add_f32 v[94:95], v[178:179], v[94:95]
	v_pk_add_f32 v[80:81], v[180:181], v[80:81]
	v_pk_add_f32 v[78:79], v[178:179], v[78:79]
	v_pk_add_f32 v[172:173], v[196:197], v[172:173]
	v_pk_add_f32 v[170:171], v[194:195], v[170:171]
	v_pk_add_f32 v[164:165], v[196:197], v[164:165]
	v_pk_add_f32 v[162:163], v[194:195], v[162:163]
	v_pk_add_f32 v[152:153], v[196:197], v[152:153]
	v_pk_add_f32 v[150:151], v[194:195], v[150:151]
	v_pk_add_f32 v[136:137], v[196:197], v[136:137]
	v_pk_add_f32 v[134:135], v[194:195], v[134:135]
	v_pk_add_f32 v[120:121], v[196:197], v[120:121]
	v_pk_add_f32 v[118:119], v[194:195], v[118:119]
	v_pk_add_f32 v[104:105], v[196:197], v[104:105]
	v_pk_add_f32 v[102:103], v[194:195], v[102:103]
	v_pk_add_f32 v[88:89], v[196:197], v[88:89]
	v_pk_add_f32 v[86:87], v[194:195], v[86:87]
	global_store_dwordx4 v[206:207], v[174:177], off
	global_store_dwordx4 v[208:209], v[166:169], off
	global_store_dwordx4 v[210:211], v[154:157], off
	global_store_dwordx4 v[212:213], v[138:141], off
	global_store_dwordx4 v[214:215], v[126:129], off
	global_store_dwordx4 v[216:217], v[110:113], off
	global_store_dwordx4 v[218:219], v[94:97], off
	global_store_dwordx4 v[220:221], v[78:81], off
	global_store_dwordx4 v[206:207], v[170:173], off offset:64
	global_store_dwordx4 v[208:209], v[162:165], off offset:64
	global_store_dwordx4 v[210:211], v[150:153], off offset:64
	global_store_dwordx4 v[212:213], v[134:137], off offset:64
	global_store_dwordx4 v[214:215], v[118:121], off offset:64
	global_store_dwordx4 v[216:217], v[102:105], off offset:64
	global_store_dwordx4 v[218:219], v[86:89], off offset:64
	global_store_dwordx4 v[220:221], v[66:69], off offset:64
	s_waitcnt vmcnt(17)
	v_pk_add_f32 v[60:61], v[200:201], v[60:61]
	v_pk_add_f32 v[58:59], v[198:199], v[58:59]
	v_pk_add_f32 v[68:69], v[200:201], v[160:161]
	v_pk_add_f32 v[66:67], v[198:199], v[158:159]
	global_store_dwordx4 v[206:207], v[66:69], off offset:128
	global_store_dwordx4 v[220:221], v[58:61], off offset:128
	s_waitcnt vmcnt(18)
	v_pk_add_f32 v[52:53], v[204:205], v[52:53]
	v_pk_add_f32 v[68:69], v[200:201], v[148:149]
	v_pk_add_f32 v[66:67], v[198:199], v[146:147]
	v_pk_add_f32 v[60:61], v[204:205], v[144:145]
	v_pk_add_f32 v[58:59], v[202:203], v[142:143]
	global_store_dwordx4 v[208:209], v[66:69], off offset:128
	global_store_dwordx4 v[206:207], v[58:61], off offset:192
	v_pk_add_f32 v[50:51], v[202:203], v[50:51]
	v_pk_add_f32 v[68:69], v[200:201], v[132:133]
	v_pk_add_f32 v[66:67], v[198:199], v[130:131]
	v_pk_add_f32 v[60:61], v[204:205], v[124:125]
	v_pk_add_f32 v[58:59], v[202:203], v[122:123]
	global_store_dwordx4 v[210:211], v[66:69], off offset:128
	global_store_dwordx4 v[208:209], v[58:61], off offset:192
	v_pk_add_f32 v[56:57], v[204:205], v[56:57]
	v_pk_add_f32 v[68:69], v[200:201], v[116:117]
	v_pk_add_f32 v[66:67], v[198:199], v[114:115]
	v_pk_add_f32 v[60:61], v[204:205], v[108:109]
	v_pk_add_f32 v[58:59], v[202:203], v[106:107]
	global_store_dwordx4 v[212:213], v[66:69], off offset:128
	global_store_dwordx4 v[210:211], v[58:61], off offset:192
	v_pk_add_f32 v[54:55], v[202:203], v[54:55]
	v_pk_add_f32 v[68:69], v[200:201], v[100:101]
	v_pk_add_f32 v[66:67], v[198:199], v[98:99]
	v_pk_add_f32 v[60:61], v[204:205], v[92:93]
	v_pk_add_f32 v[58:59], v[202:203], v[90:91]
	global_store_dwordx4 v[214:215], v[66:69], off offset:128
	global_store_dwordx4 v[212:213], v[58:61], off offset:192
	global_store_dwordx4 v[220:221], v[50:53], off offset:192
	v_pk_add_f32 v[68:69], v[200:201], v[84:85]
	v_pk_add_f32 v[66:67], v[198:199], v[82:83]
	v_pk_add_f32 v[60:61], v[204:205], v[76:77]
	v_pk_add_f32 v[58:59], v[202:203], v[74:75]
	global_store_dwordx4 v[216:217], v[66:69], off offset:128
	global_store_dwordx4 v[214:215], v[58:61], off offset:192
	v_mov_b32_e32 v50, 0
	v_pk_add_f32 v[68:69], v[200:201], v[72:73]
	v_pk_add_f32 v[66:67], v[198:199], v[70:71]
	v_pk_add_f32 v[60:61], v[204:205], v[64:65]
	v_pk_add_f32 v[58:59], v[202:203], v[62:63]
	global_store_dwordx4 v[218:219], v[66:69], off offset:128
	global_store_dwordx4 v[216:217], v[58:61], off offset:192
	global_store_dwordx4 v[218:219], v[54:57], off offset:192
	v_mov_b32_e32 v51, v50
	v_mov_b32_e32 v52, v50
	v_mov_b32_e32 v53, v50
	v_mov_b32_e32 v58, v50
	v_mov_b32_e32 v59, v50
	v_mov_b32_e32 v60, v50
	v_mov_b32_e32 v61, v50
	v_mov_b32_e32 v66, v50
	v_mov_b32_e32 v67, v50
	v_mov_b32_e32 v68, v50
	v_mov_b32_e32 v69, v50
	v_mov_b32_e32 v78, v50
	v_mov_b32_e32 v79, v50
	v_mov_b32_e32 v80, v50
	v_mov_b32_e32 v81, v50
	v_mov_b32_e32 v54, v50
	v_mov_b32_e32 v55, v50
	v_mov_b32_e32 v56, v50
	v_mov_b32_e32 v57, v50
	v_mov_b32_e32 v70, v50
	v_mov_b32_e32 v71, v50
	v_mov_b32_e32 v72, v50
	v_mov_b32_e32 v73, v50
	v_mov_b32_e32 v86, v50
	v_mov_b32_e32 v87, v50
	v_mov_b32_e32 v88, v50
	v_mov_b32_e32 v89, v50
	v_mov_b32_e32 v94, v50
	v_mov_b32_e32 v95, v50
	v_mov_b32_e32 v96, v50
	v_mov_b32_e32 v97, v50
	v_mov_b32_e32 v62, v50
	v_mov_b32_e32 v63, v50
	v_mov_b32_e32 v64, v50
	v_mov_b32_e32 v65, v50
	v_mov_b32_e32 v82, v50
	v_mov_b32_e32 v83, v50
	v_mov_b32_e32 v84, v50
	v_mov_b32_e32 v85, v50
	v_mov_b32_e32 v102, v50
	v_mov_b32_e32 v103, v50
	v_mov_b32_e32 v104, v50
	v_mov_b32_e32 v105, v50
	v_mov_b32_e32 v110, v50
	v_mov_b32_e32 v111, v50
	v_mov_b32_e32 v112, v50
	v_mov_b32_e32 v113, v50
	v_mov_b32_e32 v74, v50
	v_mov_b32_e32 v75, v50
	v_mov_b32_e32 v76, v50
	v_mov_b32_e32 v77, v50
	v_mov_b32_e32 v98, v50
	v_mov_b32_e32 v99, v50
	v_mov_b32_e32 v100, v50
	v_mov_b32_e32 v101, v50
	v_mov_b32_e32 v118, v50
	v_mov_b32_e32 v119, v50
	v_mov_b32_e32 v120, v50
	v_mov_b32_e32 v121, v50
	v_mov_b32_e32 v126, v50
	v_mov_b32_e32 v127, v50
	v_mov_b32_e32 v128, v50
	v_mov_b32_e32 v129, v50
	v_mov_b32_e32 v90, v50
	v_mov_b32_e32 v91, v50
	v_mov_b32_e32 v92, v50
	v_mov_b32_e32 v93, v50
	v_mov_b32_e32 v114, v50
	v_mov_b32_e32 v115, v50
	v_mov_b32_e32 v116, v50
	v_mov_b32_e32 v117, v50
	v_mov_b32_e32 v134, v50
	v_mov_b32_e32 v135, v50
	v_mov_b32_e32 v136, v50
	v_mov_b32_e32 v137, v50
	v_mov_b32_e32 v138, v50
	v_mov_b32_e32 v139, v50
	v_mov_b32_e32 v140, v50
	v_mov_b32_e32 v141, v50
	v_mov_b32_e32 v106, v50
	v_mov_b32_e32 v107, v50
	v_mov_b32_e32 v108, v50
	v_mov_b32_e32 v109, v50
	v_mov_b32_e32 v130, v50
	v_mov_b32_e32 v131, v50
	v_mov_b32_e32 v132, v50
	v_mov_b32_e32 v133, v50
	v_mov_b32_e32 v150, v50
	v_mov_b32_e32 v151, v50
	v_mov_b32_e32 v152, v50
	v_mov_b32_e32 v153, v50
	v_mov_b32_e32 v154, v50
	v_mov_b32_e32 v155, v50
	v_mov_b32_e32 v156, v50
	v_mov_b32_e32 v157, v50
	v_mov_b32_e32 v122, v50
	v_mov_b32_e32 v123, v50
	v_mov_b32_e32 v124, v50
	v_mov_b32_e32 v125, v50
	v_mov_b32_e32 v146, v50
	v_mov_b32_e32 v147, v50
	v_mov_b32_e32 v148, v50
	v_mov_b32_e32 v149, v50
	v_mov_b32_e32 v162, v50
	v_mov_b32_e32 v163, v50
	v_mov_b32_e32 v164, v50
	v_mov_b32_e32 v165, v50
	v_mov_b32_e32 v166, v50
	v_mov_b32_e32 v167, v50
	v_mov_b32_e32 v168, v50
	v_mov_b32_e32 v169, v50
	v_mov_b32_e32 v142, v50
	v_mov_b32_e32 v143, v50
	v_mov_b32_e32 v144, v50
	v_mov_b32_e32 v145, v50
	v_mov_b32_e32 v158, v50
	v_mov_b32_e32 v159, v50
	v_mov_b32_e32 v160, v50
	v_mov_b32_e32 v161, v50
	v_mov_b32_e32 v170, v50
	v_mov_b32_e32 v171, v50
	v_mov_b32_e32 v172, v50
	v_mov_b32_e32 v173, v50
	v_mov_b32_e32 v174, v50
	v_mov_b32_e32 v175, v50
	v_mov_b32_e32 v176, v50
	v_mov_b32_e32 v177, v50
	s_branch .LBB1_3
.LBB1_6:
	s_movk_i32 s0, 0x100
	v_cmp_gt_u32_e32 vcc, s0, v0
	s_and_saveexec_b64 s[0:1], vcc
	s_cbranch_execz .LBB1_8
	s_barrier
.LBB1_8:
	s_endpgm
	.section	.rodata,"a",@progbits
	.p2align	6, 0x0
	.amdhsa_kernel _Z11gemm_kernelPKfPKDF16bS0_Pf
		.amdhsa_group_segment_fixed_size 131072
		.amdhsa_private_segment_fixed_size 0
		.amdhsa_kernarg_size 32
		.amdhsa_user_sgpr_count 2
		.amdhsa_user_sgpr_dispatch_ptr 0
		.amdhsa_user_sgpr_queue_ptr 0
		.amdhsa_user_sgpr_kernarg_segment_ptr 1
		.amdhsa_user_sgpr_dispatch_id 0
		.amdhsa_user_sgpr_kernarg_preload_length 0
		.amdhsa_user_sgpr_kernarg_preload_offset 0
		.amdhsa_user_sgpr_private_segment_size 0
		.amdhsa_uses_dynamic_stack 0
		.amdhsa_enable_private_segment 0
		.amdhsa_system_sgpr_workgroup_id_x 1
		.amdhsa_system_sgpr_workgroup_id_y 0
		.amdhsa_system_sgpr_workgroup_id_z 0
		.amdhsa_system_sgpr_workgroup_info 0
		.amdhsa_system_vgpr_workitem_id 0
		.amdhsa_next_free_vgpr 240
		.amdhsa_next_free_sgpr 96
		.amdhsa_accum_offset 240
		.amdhsa_reserve_vcc 1
		.amdhsa_float_round_mode_32 0
		.amdhsa_float_round_mode_16_64 0
		.amdhsa_float_denorm_mode_32 3
		.amdhsa_float_denorm_mode_16_64 3
		.amdhsa_dx10_clamp 1
		.amdhsa_ieee_mode 1
		.amdhsa_fp16_overflow 0
		.amdhsa_tg_split 0
		.amdhsa_exception_fp_ieee_invalid_op 0
		.amdhsa_exception_fp_denorm_src 0
		.amdhsa_exception_fp_ieee_div_zero 0
		.amdhsa_exception_fp_ieee_overflow 0
		.amdhsa_exception_fp_ieee_underflow 0
		.amdhsa_exception_fp_ieee_inexact 0
		.amdhsa_exception_int_div_zero 0
	.end_amdhsa_kernel

amdhsa.kernels:
  - .agpr_count:     0
    .args:
      - .actual_access:  read_only
        .address_space:  global
        .offset:         0
        .size:           8
        .value_kind:     global_buffer
      - .actual_access:  read_only
        .address_space:  global
        .offset:         8
        .size:           8
        .value_kind:     global_buffer
      - .actual_access:  write_only
        .address_space:  global
        .offset:         16
        .size:           8
        .value_kind:     global_buffer
      - .actual_access:  write_only
        .address_space:  global
        .offset:         24
        .size:           8
        .value_kind:     global_buffer
    .group_segment_fixed_size: 0
    .kernarg_segment_align: 8
    .kernarg_segment_size: 32
    .language:       OpenCL C
    .language_version:
      - 2
      - 0
    .max_flat_workgroup_size: 256
    .name:           _Z11prep_kernelPKfS0_PDF16bPf
    .private_segment_fixed_size: 0
    .sgpr_count:     12
    .sgpr_spill_count: 0
    .symbol:         _Z11prep_kernelPKfS0_PDF16bPf.kd
    .uniform_work_group_size: 1
    .uses_dynamic_stack: false
    .vgpr_count:     16
    .vgpr_spill_count: 0
    .wavefront_size: 64
  - .agpr_count:     0
    .args:
      - .actual_access:  read_only
        .address_space:  global
        .offset:         0
        .size:           8
        .value_kind:     global_buffer
      - .actual_access:  read_only
        .address_space:  global
        .offset:         8
        .size:           8
        .value_kind:     global_buffer
      - .actual_access:  read_only
        .address_space:  global
        .offset:         16
        .size:           8
        .value_kind:     global_buffer
      - .actual_access:  write_only
        .address_space:  global
        .offset:         24
        .size:           8
        .value_kind:     global_buffer
    .group_segment_fixed_size: 131072
    .kernarg_segment_align: 8
    .kernarg_segment_size: 32
    .language:       OpenCL C
    .language_version:
      - 2
      - 0
    .max_flat_workgroup_size: 512
    .name:           _Z11gemm_kernelPKfPKDF16bS0_Pf
    .private_segment_fixed_size: 0
    .sgpr_count:     30
    .sgpr_spill_count: 0
    .symbol:         _Z11gemm_kernelPKfPKDF16bS0_Pf.kd
    .uniform_work_group_size: 1
    .uses_dynamic_stack: false
    .vgpr_count:     240
    .vgpr_spill_count: 0
    .wavefront_size: 64
